# attention loop: exact vmcnt counts around the MoE-down weight-conversion loads (in-order queue) instead of compiler-conservative ones; keeps KV and weight loads in flight
# speedup vs baseline: 1.0042x; 1.0042x over previous
; __device__ __forceinline__ void attn_unit(LAS unsigned char* lds, const unsigned char* Q, const unsigned char* KV, const bf16_t* KPE, const float* CST, bf16_t* O, int b, int h, int qb, CvtState& cs) {
;     ...
;     for (int t = 0; t < NT; ++t) {
;         if (t + 1 < NT) ATT_LOAD(t + 1);
.LBB0_1028:
	s_add_i32 s88, s89, 1
	s_cmp_lt_u32 s88, s33
	s_cselect_b64 s[44:45], -1, 0
	s_cmp_ge_u32 s88, s33
	s_cbranch_scc1 .LBB0_1043
	v_lshl_add_u64 v[74:75], s[12:13], 0, v[190:191]
	v_add_co_u32_e32 v74, vcc, 0x20000, v74
	s_waitcnt vmcnt(8)
	v_mov_b32_e32 v207, v191
	v_addc_co_u32_e32 v75, vcc, 0, v75, vcc
	global_load_dwordx2 v[196:197], v190, s[12:13]
	global_load_dwordx2 v[198:199], v[74:75], off
	global_load_dwordx4 v[154:157], v216, s[4:5]
	v_lshl_add_u64 v[74:75], s[12:13], 0, v[206:207]
	v_add_co_u32_e32 v76, vcc, 0x1000, v74
	global_load_dword v193, v206, s[12:13]
	s_nop 0
	v_addc_co_u32_e32 v77, vcc, 0, v75, vcc
	global_load_dword v195, v[76:77], off
	v_add_co_u32_e32 v76, vcc, 0x2000, v74
	s_nop 1
	v_addc_co_u32_e32 v77, vcc, 0, v75, vcc
	v_add_co_u32_e32 v74, vcc, 0x3000, v74
	global_load_dword v207, v[76:77], off
	s_nop 0
	v_addc_co_u32_e32 v75, vcc, 0, v75, vcc
	global_load_dword v211, v[74:75], off
	s_andn2_b64 vcc, exec, s[46:47]
	s_cbranch_vccz .LBB0_1044

;     __device__ __forceinline__ bool next(int i, Unit& u) const { if (!T.tile(i, u.pm, u.pn)) return false; u.aoff = (size_t)u.pm * atile; u.boff = (size_t)u.pn * btile; return true; }
;     __device__ __forceinline__ bool next(int i, Unit& u) const { if (!T.tile(i, u.pm, u.pn)) return false; u.aoff = (size_t)u.pm * 256 * D * 2 + (size_t)(u.pn >> 1) * 512; u.boff = (size_t)u.pn * 256 * 256 * 2; return true; }
;     __device__ __forceinline__ bool next(int i, Unit& u) const { if (!T.tile(i, u.pm, u.pn)) return false; const int e = tile_e[u.pm] & 7; u.aoff = (size_t)u.pm * atile; u.boff = ((size_t)e * nN + u.pn) * btile; return true; }
; __device__ __forceinline__ void cvt_load(const CvtState& cs, int lane, f32x4 (&v)[8]) {
;     const int kb = cs.next % CV_KB, tmp = cs.next / CV_KB, nb = tmp % CV_NB, e = tmp / CV_NB;
;     const float* src = cs.W + ((size_t)e * FF + (size_t)(128 * kb + 8 * (lane >> 2))) * D + 16 * nb + 4 * (lane & 3);
; #pragma unroll
;     for (int i = 0; i < 8; ++i) v[i] = *(const f32x4*)(src + (size_t)i * D);
; }
; __device__ __forceinline__ void attn_unit(LAS unsigned char* lds, const unsigned char* Q, const unsigned char* KV, const bf16_t* KPE, const float* CST, bf16_t* O, int b, int h, int qb, CvtState& cs) {
;     ...
;         if (kb0 <= qlo + 31) {
;             const unsigned ka = (unsigned)(uintptr_t)lds + (unsigned)((t & 1) * KBUF + r32 * KROW + hi * 32);
;             f32x16 p0, p1;
; #pragma unroll
;             for (int r = 0; r < 16; ++r) { p0[r] = 0.f; p1[r] = 0.f; }
;             { v4i k0, k1, k2, k3, k4, k5, k6, k7, k8, k9, k10, k11;
;               DSR(k0, ka, 0); DSR(k1, ka, 16); DSR(k2, ka, 32 * KROW); DSR(k3, ka, 32 * KROW + 16);
;               DSR(k4, ka, 64); DSR(k5, ka, 80); DSR(k6, ka, 32 * KROW + 64); DSR(k7, ka, 32 * KROW + 80);
;               DSR(k8, ka, 128); DSR(k9, ka, 144); DSR(k10, ka, 32 * KROW + 128); DSR(k11, ka, 32 * KROW + 144);
;               DSW4(8, k0, k1, k2, k3);
;               p0 = MMA8(CAT8(k0, k1), qf[0], p0); p1 = MMA8(CAT8(k2, k3), qf[0], p1);
;               PV_READ(vs);
;               DSW4(12, k4, k5, k6, k7);
;               p0 = MMA8(CAT8(k4, k5), qf[1], p0); p1 = MMA8(CAT8(k6, k7), qf[1], p1);
;               DSW4(8, k8, k9, k10, k11);
;               p0 = MMA8(CAT8(k8, k9), qf[2], p0); p1 = MMA8(CAT8(k10, k11), qf[2], p1); }
;             if (cvt_now) cvt_load(cs, lane, cv);
.LBB0_1034:
	s_andn2_b64 vcc, exec, s[48:49]
	s_cbranch_vccnz .LBB0_1047
	s_bitcmp1_b32 s89, 0
	s_cselect_b32 s18, 0x3400, 0
	v_add_u32_e32 v82, s18, v213
	ds_read_b128 v[66:69], v82 offset:0
	ds_read_b128 v[70:73], v82 offset:16
	ds_read_b128 v[74:77], v82 offset:0x1a00
	ds_read_b128 v[78:81], v82 offset:0x1a10
	ds_read_b128 v[218:221], v82 offset:64
	ds_read_b128 v[222:225], v82 offset:0x50
	ds_read_b128 v[226:229], v82 offset:0x1a40
	ds_read_b128 v[230:233], v82 offset:0x1a50
	ds_read_b128 v[234:237], v82 offset:0x80
	ds_read_b128 v[238:241], v82 offset:0x90
	ds_read_b128 v[242:245], v82 offset:0x1a80
	ds_read_b128 v[246:249], v82 offset:0x1a90
	s_nop 0
	s_waitcnt lgkmcnt(8)
	s_mul_i32 s18, s79, 0x2800
	v_mfma_f32_32x32x64_f8f6f4 v[82:97], v[66:73], v[98:105], 0
	v_add_u32_e32 v126, s18, v214
	ds_read_b128 v[146:149], v126 offset:0
	ds_read_b128 v[150:153], v126 offset:16
	ds_read_b128 v[138:141], v126 offset:0xa00
	ds_read_b128 v[142:145], v126 offset:0xa10
	ds_read_b128 v[130:133], v126 offset:0x1400
	ds_read_b128 v[134:137], v126 offset:0x1410
	ds_read_b128 v[122:125], v126 offset:0x1e00
	ds_read_b128 v[126:129], v126 offset:0x1e10
	s_waitcnt lgkmcnt(12)
	s_waitcnt lgkmcnt(8)
	s_andn2_b64 vcc, exec, s[46:47]
	v_mfma_f32_32x32x64_f8f6f4 v[66:81], v[74:81], v[98:105], 0
	v_mfma_f32_32x32x64_f8f6f4 v[82:97], v[218:225], v[106:113], v[82:97]
	v_mfma_f32_32x32x64_f8f6f4 v[66:81], v[226:233], v[106:113], v[66:81]
	v_mfma_f32_32x32x64_f8f6f4 v[82:97], v[234:241], v[114:121], v[82:97]
	v_mfma_f32_32x32x64_f8f6f4 v[66:81], v[242:249], v[114:121], v[66:81]
	s_cbranch_vccnz .LBB0_1037
	s_mul_hi_i32 s18, s35, 0x92492493
	s_add_i32 s18, s18, s35
	s_ashr_i32 s19, s18, 5
	s_lshr_b32 s20, s18, 31
	s_add_i32 s19, s19, s20
	s_mul_i32 s21, s19, 56
	s_ashr_i32 s48, s19, 31
	s_sub_i32 s21, s35, s21
	s_lshr_b32 s48, s48, 25
	s_add_i32 s48, s19, s48
	s_ashr_i32 s18, s18, 12
	s_waitcnt vmcnt(7)
	v_lshl_or_b32 v158, s21, 7, v204
	s_and_b32 s48, s48, 0xfffff80
	s_add_i32 s18, s18, s20
	v_ashrrev_i32_e32 v159, 31, v158
	s_sub_i32 s48, s19, s48
	v_mad_i64_i32 v[158:159], s[18:19], s18, v208, v[158:159]
	v_lshlrev_b64 v[158:159], 13, v[158:159]
	s_lshl_b32 s18, s48, 4
	v_lshl_add_u64 v[158:159], s[26:27], 0, v[158:159]
	s_ashr_i32 s19, s18, 31
	v_lshl_add_u64 v[158:159], s[18:19], 2, v[158:159]
	v_lshlrev_b32_e32 v160, 2, v202
	v_mov_b32_e32 v161, v191
	s_waitcnt vmcnt(7)
	v_lshl_add_u64 v[182:183], v[158:159], 0, v[160:161]
	v_add_co_u32_e32 v162, vcc, s52, v182
	s_nop 1
	v_addc_co_u32_e32 v163, vcc, 0, v183, vcc
	v_add_co_u32_e32 v166, vcc, s62, v182
	global_load_dwordx4 v[158:161], v[182:183], off
	s_nop 0
	global_load_dwordx4 v[162:165], v[162:163], off
	v_addc_co_u32_e32 v167, vcc, 0, v183, vcc
	v_add_co_u32_e32 v170, vcc, s63, v182
	s_nop 1
	v_addc_co_u32_e32 v171, vcc, 0, v183, vcc
	v_add_co_u32_e32 v174, vcc, s64, v182
	global_load_dwordx4 v[166:169], v[166:167], off
	s_nop 0
	global_load_dwordx4 v[170:173], v[170:171], off
	v_addc_co_u32_e32 v175, vcc, 0, v183, vcc
	v_add_co_u32_e32 v178, vcc, s65, v182
	s_nop 1
	v_addc_co_u32_e32 v179, vcc, 0, v183, vcc
	v_add_co_u32_e32 v184, vcc, s66, v182
	global_load_dwordx4 v[174:177], v[174:175], off
	s_nop 0
	global_load_dwordx4 v[178:181], v[178:179], off
	v_addc_co_u32_e32 v185, vcc, 0, v183, vcc
	s_waitcnt vmcnt(13)
	v_add_co_u32_e32 v186, vcc, s67, v182
	s_nop 1
	v_addc_co_u32_e32 v187, vcc, 0, v183, vcc
	global_load_dwordx4 v[182:185], v[184:185], off
	s_nop 0
	global_load_dwordx4 v[186:189], v[186:187], off

;     __device__ __forceinline__ bool next(int i, Unit& u) const { if (!T.tile(i, u.pm, u.pn)) return false; u.aoff = (size_t)u.pm * atile; u.boff = (size_t)u.pn * btile; return true; }
;     __device__ __forceinline__ bool next(int i, Unit& u) const { if (!T.tile(i, u.pm, u.pn)) return false; u.aoff = (size_t)u.pm * 256 * D * 2 + (size_t)(u.pn >> 1) * 512; u.boff = (size_t)u.pn * 256 * 256 * 2; return true; }
;     __device__ __forceinline__ bool next(int i, Unit& u) const { if (!T.tile(i, u.pm, u.pn)) return false; const int e = tile_e[u.pm] & 7; u.aoff = (size_t)u.pm * atile; u.boff = ((size_t)e * nN + u.pn) * btile; return true; }
; __device__ __forceinline__ void cvt_store(CvtState& cs, int lane, const f32x4 (&v)[8]) {
;     const int kb = cs.next % CV_KB, tmp = cs.next / CV_KB, nb = tmp % CV_NB, e = tmp / CV_NB;
;     unsigned char* dst = cs.WT + ((size_t)e * D + (size_t)(16 * nb + 4 * (lane & 3))) * FF + 128 * kb + 8 * (lane >> 2);
; #pragma unroll
;     for (int j = 0; j < 4; ++j) { u32x2 w; w.x = pk4_fp8(v[0][j] * CV_WS, v[1][j] * CV_WS, v[2][j] * CV_WS, v[3][j] * CV_WS); w.y = pk4_fp8(v[4][j] * CV_WS, v[5][j] * CV_WS, v[6][j] * CV_WS, v[7][j] * CV_WS);
;         *(u32x2*)(dst + (size_t)j * FF) = w; }
;     ++cs.next;
; }
; __device__ __forceinline__ void attn_unit(LAS unsigned char* lds, const unsigned char* Q, const unsigned char* KV, const bf16_t* KPE, const float* CST, bf16_t* O, int b, int h, int qb, CvtState& cs) {
;     ...
;         if (cvt_pend) { cvt_store(cs, lane, cv); cvt_pend = false; }
.LBB0_1043:
	s_andn2_b64 vcc, exec, s[46:47]
	s_cbranch_vccnz .LBB0_1030
	s_waitcnt vmcnt(0)
.LBB0_1044:
	s_mul_hi_i32 s18, s35, 0x92492493
	s_add_i32 s18, s18, s35
	s_ashr_i32 s19, s18, 5
	s_lshr_b32 s20, s18, 31
	s_add_i32 s19, s19, s20
	s_ashr_i32 s46, s19, 31
	s_lshr_b32 s46, s46, 25
	s_add_i32 s46, s19, s46
	s_and_b32 s46, s46, 0xfffff80
	s_ashr_i32 s18, s18, 12
	s_sub_i32 s46, s19, s46
	s_add_i32 s18, s18, s20
	s_mul_i32 s21, s19, 56
	s_ashr_i32 s19, s18, 31
	v_lshl_or_b32 v74, s46, 4, v202
	s_lshl_b64 s[18:19], s[18:19], 11
	v_ashrrev_i32_e32 v75, 31, v74
	v_lshl_add_u64 v[74:75], s[18:19], 0, v[74:75]
	v_mov_b64_e32 v[76:77], s[30:31]
	v_mad_u64_u32 v[76:77], s[18:19], v74, s61, v[76:77]
	v_mad_i32_i24 v77, v75, s61, v77
	s_waitcnt vmcnt(14)
	v_mul_f32_e32 v74, 0x42800000, v158
	s_waitcnt vmcnt(13)
	v_mul_f32_e32 v75, 0x42800000, v162
	v_med3_f32 v79, v74, s53, v203
	v_med3_f32 v75, v75, s53, v203
	v_mov_b32_e32 v74, v191
	v_cvt_pk_fp8_f32 v74, v79, v75
	s_waitcnt vmcnt(12)
	v_mul_f32_e32 v78, 0x42800000, v166
	s_waitcnt vmcnt(11)
	v_mul_f32_e32 v75, 0x42800000, v170
	v_med3_f32 v78, v78, s53, v203
	v_med3_f32 v75, v75, s53, v203
	v_cvt_pk_fp8_f32 v74, v78, v75 op_sel:[0,0,1]
	s_waitcnt vmcnt(10)
	v_mul_f32_e32 v75, 0x42800000, v174
	s_waitcnt vmcnt(9)
	v_mul_f32_e32 v78, 0x42800000, v178
	v_med3_f32 v80, v75, s53, v203
	v_med3_f32 v78, v78, s53, v203
	v_mov_b32_e32 v75, v191
	v_cvt_pk_fp8_f32 v75, v80, v78
	s_waitcnt vmcnt(8)
	v_mul_f32_e32 v79, 0x42800000, v182
	s_waitcnt vmcnt(7)
	v_mul_f32_e32 v78, 0x42800000, v186
	s_sub_i32 s21, s35, s21
	v_med3_f32 v79, v79, s53, v203
	v_med3_f32 v78, v78, s53, v203
	s_lshl_b32 s18, s21, 7
	v_cvt_pk_fp8_f32 v75, v79, v78 op_sel:[0,0,1]
	s_ashr_i32 s19, s18, 31
	v_lshl_add_u64 v[76:77], v[76:77], 0, s[18:19]
	v_lshl_add_u64 v[76:77], v[76:77], 0, v[204:205]
	global_store_dwordx2 v[76:77], v[74:75], off
	v_mul_f32_e32 v74, 0x42800000, v159
	v_mul_f32_e32 v75, 0x42800000, v163
	v_med3_f32 v79, v74, s53, v203
	v_med3_f32 v75, v75, s53, v203
	v_mov_b32_e32 v74, v191
	v_cvt_pk_fp8_f32 v74, v79, v75
	v_mul_f32_e32 v78, 0x42800000, v167
	v_mul_f32_e32 v75, 0x42800000, v171
	v_med3_f32 v78, v78, s53, v203
	v_med3_f32 v75, v75, s53, v203
	v_cvt_pk_fp8_f32 v74, v78, v75 op_sel:[0,0,1]
	v_mul_f32_e32 v75, 0x42800000, v175
	v_mul_f32_e32 v78, 0x42800000, v179
	v_med3_f32 v80, v75, s53, v203
	v_med3_f32 v78, v78, s53, v203
	v_mov_b32_e32 v75, v191
	v_cvt_pk_fp8_f32 v75, v80, v78
	v_mul_f32_e32 v79, 0x42800000, v183
	v_mul_f32_e32 v78, 0x42800000, v187
	v_med3_f32 v79, v79, s53, v203
	v_med3_f32 v78, v78, s53, v203
	v_cvt_pk_fp8_f32 v75, v79, v78 op_sel:[0,0,1]
	s_movk_i32 s18, 0x1000
	v_add_co_u32_e32 v78, vcc, s18, v76
	s_add_i32 s35, s35, 1
	s_nop 0
	v_addc_co_u32_e32 v79, vcc, 0, v77, vcc
	global_store_dwordx2 v[78:79], v[74:75], off offset:3072
	v_mul_f32_e32 v74, 0x42800000, v160
	v_mul_f32_e32 v75, 0x42800000, v164
	v_med3_f32 v79, v74, s53, v203
	v_med3_f32 v75, v75, s53, v203
	v_mov_b32_e32 v74, v191
	v_cvt_pk_fp8_f32 v74, v79, v75
	v_mul_f32_e32 v78, 0x42800000, v168
	v_mul_f32_e32 v75, 0x42800000, v172
	v_med3_f32 v78, v78, s53, v203
	v_med3_f32 v75, v75, s53, v203
	v_cvt_pk_fp8_f32 v74, v78, v75 op_sel:[0,0,1]
	v_mul_f32_e32 v75, 0x42800000, v176
	v_mul_f32_e32 v78, 0x42800000, v180
	v_med3_f32 v80, v75, s53, v203
	v_med3_f32 v78, v78, s53, v203
	v_mov_b32_e32 v75, v191
	v_cvt_pk_fp8_f32 v75, v80, v78
	v_mul_f32_e32 v79, 0x42800000, v184
	v_mul_f32_e32 v78, 0x42800000, v188
	v_med3_f32 v79, v79, s53, v203
	v_med3_f32 v78, v78, s53, v203
	v_cvt_pk_fp8_f32 v75, v79, v78 op_sel:[0,0,1]
	v_add_co_u32_e32 v78, vcc, s55, v76
	s_nop 1
	v_addc_co_u32_e32 v79, vcc, 0, v77, vcc
	global_store_dwordx2 v[78:79], v[74:75], off offset:2048
	v_mul_f32_e32 v74, 0x42800000, v161
	v_mul_f32_e32 v75, 0x42800000, v165
	v_med3_f32 v79, v74, s53, v203
	v_med3_f32 v75, v75, s53, v203
	v_mov_b32_e32 v74, v191
	v_cvt_pk_fp8_f32 v74, v79, v75
	v_mul_f32_e32 v78, 0x42800000, v169
	v_mul_f32_e32 v75, 0x42800000, v173
	v_med3_f32 v78, v78, s53, v203
	v_med3_f32 v75, v75, s53, v203
	v_cvt_pk_fp8_f32 v74, v78, v75 op_sel:[0,0,1]
	v_mul_f32_e32 v75, 0x42800000, v177
	v_mul_f32_e32 v78, 0x42800000, v181
	v_med3_f32 v80, v75, s53, v203
	v_med3_f32 v78, v78, s53, v203
	v_mov_b32_e32 v75, v191
	v_cvt_pk_fp8_f32 v75, v80, v78
	v_mul_f32_e32 v79, 0x42800000, v185
	v_mul_f32_e32 v78, 0x42800000, v189
	v_med3_f32 v79, v79, s53, v203
	v_med3_f32 v78, v78, s53, v203
	v_cvt_pk_fp8_f32 v75, v79, v78 op_sel:[0,0,1]
	v_add_co_u32_e32 v76, vcc, 0x5000, v76
	s_nop 1
	v_addc_co_u32_e32 v77, vcc, 0, v77, vcc
	global_store_dwordx2 v[76:77], v[74:75], off offset:1024
	s_and_b64 s[18:19], s[38:39], s[42:43]
	s_andn2_b64 vcc, exec, s[18:19]
	s_cbranch_vccz .LBB0_1031
	s_branch .LBB0_1032

; __device__ __forceinline__ void attn_unit(LAS unsigned char* lds, const unsigned char* Q, const unsigned char* KV, const bf16_t* KPE, const float* CST, bf16_t* O, int b, int h, int qb, CvtState& cs) {
;     ...
;         const int vn = (vs == 2) ? 0 : vs + 1;
;         if (t + 1 < NT) ATT_WRITE((t + 1) & 1, vn);
.LBB0_1047:
	s_add_i32 s18, s79, 1
	s_cmp_lg_u32 s79, 2
	s_cselect_b32 s79, s18, 0
	s_andn2_b64 vcc, exec, s[44:45]
	s_cbranch_vccnz .LBB0_1049
	s_andn2_b64 vcc, exec, s[46:47]
	s_cbranch_vccnz .Lmy_attw_plain
	s_bitcmp1_b32 s88, 0
	s_cselect_b32 s18, 0x3400, 0
	s_add_i32 s18, s18, 0
	v_add_u32_e32 v74, s18, v194
	s_waitcnt vmcnt(13)
	ds_write2st64_b64 v74, v[196:197], v[198:199] offset1:13
	v_mov_b32_e32 v74, v191
	v_mov_b32_e32 v75, v191
	s_waitcnt vmcnt(12)
	v_cvt_scalef32_pk_fp8_bf16 v74, v154, 1.0
	v_cvt_scalef32_pk_fp8_bf16 v75, v156, 1.0
	s_mul_i32 s19, s79, 0x2800
	v_cvt_scalef32_pk_fp8_bf16 v74, v155, 1.0 op_sel:[0,0,1]
	v_cvt_scalef32_pk_fp8_bf16 v75, v157, 1.0 op_sel:[0,0,1]
	v_add_u32_e32 v76, s18, v200
	ds_write_b64 v76, v[74:75] offset:128
	s_waitcnt vmcnt(10)
	v_perm_b32 v74, v195, v193, s56
	s_waitcnt vmcnt(8)
	v_perm_b32 v75, v211, v207, s56
	s_branch .Lmy_attw_join
.Lmy_attw_plain:
	s_bitcmp1_b32 s88, 0
	s_cselect_b32 s18, 0x3400, 0
	s_add_i32 s18, s18, 0
	v_add_u32_e32 v74, s18, v194
	s_waitcnt vmcnt(5)
	ds_write2st64_b64 v74, v[196:197], v[198:199] offset1:13
	v_mov_b32_e32 v74, v191
	v_mov_b32_e32 v75, v191
	s_waitcnt vmcnt(4)
	v_cvt_scalef32_pk_fp8_bf16 v74, v154, 1.0
	v_cvt_scalef32_pk_fp8_bf16 v75, v156, 1.0
	s_mul_i32 s19, s79, 0x2800
	v_cvt_scalef32_pk_fp8_bf16 v74, v155, 1.0 op_sel:[0,0,1]
	v_cvt_scalef32_pk_fp8_bf16 v75, v157, 1.0 op_sel:[0,0,1]
	v_add_u32_e32 v76, s18, v200
	ds_write_b64 v76, v[74:75] offset:128
	s_waitcnt vmcnt(2)
	v_perm_b32 v74, v195, v193, s56
	s_waitcnt vmcnt(0)
	v_perm_b32 v75, v211, v207, s56
.Lmy_attw_join:
	v_add_u32_e32 v79, s19, v201
	v_perm_b32 v76, v195, v193, s57
	v_perm_b32 v77, v211, v207, s57
	v_perm_b32 v78, v75, v74, s58
	v_perm_b32 v74, v75, v74, s59
	v_add_u32_e32 v75, 0x6800, v79
	ds_write2_b32 v75, v78, v74 offset1:20
	v_perm_b32 v74, v77, v76, s58
	v_perm_b32 v76, v77, v76, s59
	ds_write2_b32 v75, v74, v76 offset0:40 offset1:60
